# layer-0 KV-split point moved from tile 244 to tile 240 (partner takes 20 tiles, 16 for ctx-unit owners)
# baseline (speedup 1.0000x reference)
.Lkv_upL0:
	s_mov_b32 s28, 0x8700000
	s_movk_i32 s29, 16
	s_cmpk_gt_u32 s19, 0x10f
	s_cbranch_scc1 .LBB0_584
	s_mov_b32 s28, 0x8940000
	s_movk_i32 s29, 12
	s_branch .LBB0_584

.Lkv_loL0:
	s_movk_i32 s29, 236
	s_cmpk_gt_u32 s19, 0x10f
	s_cbranch_scc1 .LBB0_584
	s_movk_i32 s29, 240
	s_branch .LBB0_584
